# GATE/UP tile rebalance: hi CUs run one own-input UP tile before the seam barrier, 11 tile units per CU instead of 12
# speedup vs baseline: 1.0113x; 1.0113x over previous
_Z10fwd_kernel6Params:
	s_mov_b32 s100, 0
	v_writelane_b32 v255, s100, 9
	s_mov_b32 s88, s2
	s_load_dword s2, s[0:1], 0xc0
	v_cmp_gt_u32_e32 vcc, 16, v0
	s_waitcnt lgkmcnt(0)
	v_writelane_b32 v252, s2, 0
	s_add_u32 s2, s0, 0xc0
	s_addc_u32 s3, s1, 0
	v_writelane_b32 v252, s2, 1
	s_nop 1
	v_writelane_b32 v252, s3, 2
	s_and_saveexec_b64 s[2:3], vcc
	v_lshl_add_u32 v1, v0, 2, 0
	v_add_u32_e32 v1, 0x21000, v1
	v_mov_b32_e32 v2, 0
	ds_write_b32 v1, v2
	s_or_b64 exec, exec, s[2:3]
	s_load_dwordx4 s[84:87], s[0:1], 0xa8
	v_cmp_gt_u32_e32 vcc, 21, v0
	s_and_saveexec_b64 s[2:3], vcc
	s_cbranch_execz .LBB0_4
	v_lshlrev_b32_e32 v1, 3, v0
	global_load_dwordx2 v[2:3], v1, s[0:1]
	v_add_u32_e32 v1, 0, v1
	v_add_u32_e32 v1, 0x21040, v1
	s_waitcnt vmcnt(0)
	ds_write_b64 v1, v[2:3]

.LBB0_1823:
	s_cmp_lg_u32 s8, s4
	s_cbranch_scc1 .Lgate_rf_std
	s_cmp_lg_u32 s28, 0x100
	s_cbranch_scc1 .Lgate_rf_std
	s_cmpk_lt_i32 s4, 0x80
	s_cbranch_scc1 .Lgate_rf_std
	s_xor_b32 s8, s8, 8
	s_mov_b64 s[10:11], 0
	s_branch .LBB0_1824

.LBB0_1829:
	v_readfirstlane_b32 s10, v1
	s_ashr_i32 s30, s10, 6
	s_cmpk_gt_i32 s4, 0x57f
	s_waitcnt vmcnt(0) lgkmcnt(0)
	s_barrier
	s_cbranch_scc1 .LBB0_1845
	s_mov_b32 s100, s4
	s_cmp_lg_u32 s28, 0x100
	s_cbranch_scc1 .Lgate_u0_std
	s_cmpk_lt_i32 s4, 0x80
	s_cbranch_scc1 .Lgate_u0_std
	s_or_b32 s100, s4, 8
	s_bitcmp1_b32 s4, 3
	s_cselect_b32 s101, 0, 0x200
	s_add_i32 s100, s100, s101
.Lgate_u0_std:
	v_add_u32_e32 v2, 0x2000, v8
	v_ashrrev_i32_e32 v4, 31, v2
	v_lshrrev_b32_e32 v4, 22, v4
	v_add_u32_e32 v4, v2, v4
	v_ashrrev_i32_e32 v12, 10, v4
	v_mul_i32_i24_e32 v4, 0x400, v12
	v_sub_u32_e32 v2, v2, v4
	v_lshrrev_b32_e32 v4, 4, v2
	v_bitop3_b32 v2, v4, v2, 32 bitop3:0x6c
	v_ashrrev_i32_e32 v4, 31, v2
	v_lshrrev_b32_e32 v4, 26, v4
	v_add_u32_e32 v4, v2, v4
	v_lshlrev_b32_e32 v5, 3, v12
	v_ashrrev_i32_e32 v13, 6, v4
	v_and_b32_e32 v5, -16, v5
	v_add_u32_e32 v5, v13, v5
	v_and_b32_e32 v6, 3, v13
	s_mov_b32 s0, 0xfffe0
	v_lshrrev_b32_e32 v7, 2, v5
	v_lshlrev_b32_e32 v9, 1, v5
	v_and_b32_e32 v4, 0xc0, v4
	v_and_or_b32 v6, v5, s0, v6
	v_and_b32_e32 v7, 4, v7
	v_and_b32_e32 v9, 24, v9
	v_sub_u32_e32 v2, v2, v4
	v_or3_b32 v6, v6, v7, v9
	v_lshlrev_b32_e32 v7, 5, v12
	v_ashrrev_i16_sdwa v2, v228, sext(v2) dst_sel:DWORD dst_unused:UNUSED_PAD src0_sel:DWORD src1_sel:BYTE_0
	v_and_b32_e32 v7, 32, v7
	v_bfe_i32 v14, v2, 0, 16
	v_add_lshl_u32 v2, v7, v14, 1
	v_lshl_add_u32 v132, v6, 12, v2
	v_lshl_add_u32 v134, v5, 12, v2
	v_ashrrev_i32_e32 v2, 31, v8
	v_lshrrev_b32_e32 v2, 22, v2
	v_add_u32_e32 v2, v8, v2
	v_and_b32_e32 v2, 0xfffffc00, v2
	v_sub_u32_e32 v2, v8, v2
	v_ashrrev_i32_e32 v5, 31, v1
	v_lshrrev_b32_e32 v4, 4, v2
	v_lshrrev_b32_e32 v5, 26, v5
	v_bitop3_b32 v4, v4, v2, 32 bitop3:0x6c
	v_ashrrev_i32_e32 v2, 31, v2
	v_add_u32_e32 v5, v1, v5
	v_lshrrev_b32_e32 v2, 26, v2
	v_ashrrev_i32_e32 v16, 6, v5
	s_add_u32 s31, s2, 0x5000000
	v_add_u32_e32 v2, v4, v2
	v_lshlrev_b32_e32 v5, 3, v16
	s_addc_u32 s33, s3, 0
	v_ashrrev_i32_e32 v15, 6, v2
	v_and_b32_e32 v5, -16, v5
	s_add_u32 s34, s2, 0x30e00000
	v_add_u32_e32 v5, v15, v5
	v_and_b32_e32 v6, 3, v15
	s_addc_u32 s35, s3, 0
	v_and_or_b32 v6, v5, s0, v6
	s_ashr_i32 s0, s100, 31
	s_lshr_b32 s0, s0, 29
	s_add_i32 s0, s100, s0
	s_ashr_i32 s1, s0, 3
	s_and_b32 s0, s0, -8
	s_ashr_i32 s12, s10, 8
	s_lshl_b32 s11, s30, 10
	s_sub_i32 s0, s100, s0
	s_cmp_lt_i32 s0, 0
	s_movk_i32 s8, 0xb1
	s_cselect_b32 s8, s8, 0xb0
	s_mul_i32 s0, s8, s0
	s_add_i32 s0, s0, s1
	s_mul_hi_i32 s1, s0, 0x2e8ba2e9
	s_lshr_b32 s8, s1, 31
	s_ashr_i32 s1, s1, 5
	s_add_i32 s1, s1, s8
	s_lshl_b32 s9, s1, 3
	s_mulk_i32 s1, 0xb0
	s_sub_i32 s0, s0, s1
	s_bfe_u32 s1, s0, 0x3001c
	s_add_i32 s1, s0, s1
	s_sext_i32_i16 s8, s1
	s_and_b32 s1, s1, 0xfff8
	s_sub_i32 s0, s0, s1
	s_sext_i32_i16 s0, s0
	s_lshr_b32 s8, s8, 3
	s_add_i32 s20, s9, s0
	s_ashr_i32 s21, s20, 31
	s_bfe_i64 s[14:15], s[8:9], 0x100000
	s_lshl_b64 s[0:1], s[20:21], 20
	s_lshl_b64 s[14:15], s[14:15], 20
	s_add_u32 s22, s34, s14
	s_addc_u32 s23, s35, s15
	s_add_i32 s38, s72, 0x10000
	v_lshrrev_b32_e32 v7, 2, v5
	v_lshlrev_b32_e32 v8, 1, v5
	v_and_b32_e32 v2, 0xc0, v2
	s_add_i32 s39, s38, s11
	v_and_b32_e32 v7, 4, v7
	v_and_b32_e32 v8, 24, v8
	v_sub_u32_e32 v2, v4, v2
	s_add_i32 s40, s39, 0x2000
	v_or3_b32 v6, v6, v7, v8
	v_lshlrev_b32_e32 v7, 5, v16
	v_ashrrev_i16_sdwa v2, v228, sext(v2) dst_sel:DWORD dst_unused:UNUSED_PAD src0_sel:DWORD src1_sel:BYTE_0
	s_add_u32 s14, s22, 0x80000
	v_and_b32_e32 v7, 32, v7
	v_bfe_i32 v17, v2, 0, 16
	s_addc_u32 s15, s23, 0
	s_add_i32 s41, s72, 0x14000
	v_add_lshl_u32 v4, v7, v17, 1
	s_add_i32 s42, s41, s11
	v_lshl_add_u32 v2, v6, 12, v4
	s_mov_b32 m0, s39
	s_add_i32 s43, s42, 0x2000
	global_load_lds_dwordx4 v2, s[22:23]
	s_mov_b32 m0, s40
	s_add_u32 s24, s31, s0
	global_load_lds_dwordx4 v132, s[22:23]
	s_mov_b32 m0, s42
	s_addc_u32 s25, s33, s1
	s_add_i32 s44, s72, s11
	global_load_lds_dwordx4 v2, s[14:15]
	s_mov_b32 m0, s43
	s_add_i32 s45, s44, 0x2000
	v_lshl_add_u32 v136, v5, 12, v4
	global_load_lds_dwordx4 v132, s[14:15]
	s_mov_b32 m0, s44
	s_add_u32 s0, s24, 0x80000
	global_load_lds_dwordx4 v136, s[24:25]
	s_mov_b32 m0, s45
	s_addc_u32 s1, s25, 0
	s_add_i32 s46, s44, 0x4000
	global_load_lds_dwordx4 v134, s[24:25]
	s_mov_b32 m0, s46
	s_add_i32 s47, s44, 0x6000
	global_load_lds_dwordx4 v136, s[0:1]
	s_mov_b32 m0, s47
	v_mov_b32_e32 v133, v3
	global_load_lds_dwordx4 v134, s[0:1]
	v_mov_b32_e32 v137, v3
	v_mov_b32_e32 v135, v3
	s_cmp_eq_u32 s12, 1
	s_mov_b32 s64, s72
	v_lshl_add_u64 v[10:11], s[22:23], 0, v[2:3]
	v_lshl_add_u64 v[8:9], s[22:23], 0, v[132:133]
	v_lshl_add_u64 v[4:5], s[24:25], 0, v[136:137]
	s_cselect_b64 s[0:1], -1, 0
	s_cmp_lg_u32 s12, 1
	v_lshl_add_u64 v[6:7], s[24:25], 0, v[134:135]
	s_cbranch_scc1 .LBB0_1832
	s_barrier

.LBB0_1835:
	s_add_i32 s56, s56, 1
	s_mul_i32 s13, s56, s29
	s_mul_hi_u32 s15, s56, s28
	s_add_i32 s15, s15, s13
	s_mul_i32 s13, s56, s28
	s_add_u32 s16, s13, s4
	s_addc_u32 s17, s15, s5
	s_cmp_lg_u32 s28, 0x100
	s_cbranch_scc1 .Lgate_k_std
	s_cmpk_lt_i32 s4, 0x80
	s_cbranch_scc1 .Lgate_k_std
	s_cmp_gt_u32 s56, 3
	s_cbranch_scc1 .Lgate_k_std
	s_or_b32 s100, s4, 8
	s_andn2_b32 s101, s4, 8
	s_bitcmp1_b32 s56, 0
	s_cselect_b32 s100, s101, s100
	s_lshr_b32 s101, s56, 1
	s_bitcmp1_b32 s4, 3
	s_cselect_b32 s16, 0, 2
	s_add_i32 s101, s101, s16
	s_lshl_b32 s101, s101, 8
	s_add_i32 s16, s100, s101
	s_mov_b32 s17, 0
.Lgate_k_std:
	v_mov_b64_e32 v[4:5], 0x580
	v_cmp_lt_i64_e64 s[36:37], s[16:17], v[4:5]
	v_mov_b64_e32 v[4:5], 0x57f
	v_cmp_gt_i64_e32 vcc, s[16:17], v[4:5]
	s_cbranch_vccnz .LBB0_1837
	s_ashr_i32 s12, s16, 31
	s_lshr_b32 s12, s12, 29
	s_add_i32 s12, s16, s12
	s_ashr_i32 s13, s12, 3
	s_and_b32 s12, s12, -8
	s_sub_i32 s12, s16, s12
	s_cmp_lt_i32 s12, 0
	s_movk_i32 s14, 0xb1
	s_cselect_b32 s14, s14, 0xb0
	s_mul_i32 s12, s14, s12
	s_add_i32 s12, s12, s13
	s_mul_hi_i32 s13, s12, 0x2e8ba2e9
	s_lshr_b32 s14, s13, 31
	s_ashr_i32 s13, s13, 5
	s_add_i32 s13, s13, s14
	s_lshl_b32 s14, s13, 3
	s_sub_i32 s15, 64, s14
	s_min_i32 s15, s15, 8
	s_abs_i32 s16, s15
	v_cvt_f32_u32_e32 v4, s16
	s_sub_i32 s18, 0, s16
	s_mulk_i32 s13, 0xb0
	s_sub_i32 s13, s12, s13
	v_rcp_iflag_f32_e32 v4, v4
	s_abs_i32 s12, s13
	s_xor_b32 s17, s13, s15
	s_ashr_i32 s17, s17, 31
	v_mul_f32_e32 v4, 0x4f7ffffe, v4
	v_cvt_u32_f32_e32 v4, v4
	s_nop 0
	v_readfirstlane_b32 s19, v4
	s_mul_i32 s18, s18, s19
	s_mul_hi_u32 s18, s19, s18
	s_add_i32 s19, s19, s18
	s_mul_hi_u32 s18, s12, s19
	s_mul_i32 s19, s18, s16
	s_sub_i32 s12, s12, s19
	s_add_i32 s26, s18, 1
	s_sub_i32 s19, s12, s16
	s_cmp_ge_u32 s12, s16
	s_cselect_b32 s18, s26, s18
	s_cselect_b32 s12, s19, s12
	s_add_i32 s19, s18, 1
	s_cmp_ge_u32 s12, s16
	s_cselect_b32 s12, s19, s18
	s_xor_b32 s12, s12, s17
	s_sub_i32 s12, s12, s17
	s_mul_i32 s15, s12, s15
	s_sub_i32 s13, s13, s15
	s_add_i32 s14, s13, s14

.LBB0_1854:
	v_readlane_b32 s100, v255, 9
	v_readlane_b32 s101, v252, 0
	s_cmp_lg_u32 s100, 0
	s_cbranch_scc1 .Lgu_bar
	s_cmp_lg_u32 s101, 0x100
	s_cbranch_scc1 .Lgu_bar
	s_mov_b32 s100, 2
	s_cmpk_lt_i32 s88, 0x80
	s_cbranch_scc1 .Lgu_setflag
	s_mov_b32 s100, 1
	v_writelane_b32 v255, s100, 9
	s_branch .Lup_body
.Lgu_setflag:
	v_writelane_b32 v255, s100, 9

.Lup_body:
	v_mov_b32_e32 v16, v0
	v_readlane_b32 s26, v252, 0
	s_mov_b32 s27, s88
	s_mov_b64 s[6:7], s[68:69]
	s_cmpk_gt_i32 s27, 0x57f
	v_readfirstlane_b32 s9, v16
	s_cbranch_scc1 .LBB0_1927
	s_add_u32 s28, s6, 0x5000000
	s_addc_u32 s29, s7, 0
	s_add_u32 s30, s6, 0x32400000
	s_addc_u32 s31, s7, 0
	s_add_i32 s0, s72, 0x210c8
	v_mov_b32_e32 v1, s0
	s_waitcnt lgkmcnt(0)
	ds_read2_b64 v[4:7], v1 offset1:1
	v_lshlrev_b32_e32 v1, 4, v16
	v_add_u32_e32 v2, 0x2000, v1
	v_ashrrev_i32_e32 v8, 31, v2
	v_lshrrev_b32_e32 v8, 22, v8
	v_add_u32_e32 v8, v2, v8
	v_ashrrev_i32_e32 v17, 10, v8
	v_mul_i32_i24_e32 v8, 0x400, v17
	v_sub_u32_e32 v2, v2, v8
	v_lshrrev_b32_e32 v8, 4, v2
	v_bitop3_b32 v2, v8, v2, 32 bitop3:0x6c
	v_ashrrev_i32_e32 v8, 31, v2
	v_lshrrev_b32_e32 v8, 26, v8
	v_add_u32_e32 v8, v2, v8
	v_lshlrev_b32_e32 v9, 3, v17
	v_ashrrev_i32_e32 v18, 6, v8
	v_and_b32_e32 v9, -16, v9
	v_add_u32_e32 v9, v18, v9
	v_and_b32_e32 v10, 3, v18
	s_mov_b32 s0, 0xfffe0
	v_lshrrev_b32_e32 v11, 2, v9
	v_lshlrev_b32_e32 v12, 1, v9
	v_and_b32_e32 v8, 0xc0, v8
	v_and_or_b32 v10, v9, s0, v10
	v_and_b32_e32 v11, 4, v11
	v_and_b32_e32 v12, 24, v12
	v_sub_u32_e32 v2, v2, v8
	v_or3_b32 v10, v10, v11, v12
	v_lshlrev_b32_e32 v11, 5, v17
	v_ashrrev_i16_sdwa v2, v228, sext(v2) dst_sel:DWORD dst_unused:UNUSED_PAD src0_sel:DWORD src1_sel:BYTE_0
	v_and_b32_e32 v11, 32, v11
	v_bfe_i32 v19, v2, 0, 16
	v_add_lshl_u32 v2, v11, v19, 1
	v_lshl_add_u32 v172, v10, 12, v2
	v_lshl_add_u32 v174, v9, 12, v2
	v_bfe_i32 v2, v16, 27, 1
	v_lshrrev_b32_e32 v2, 22, v2
	v_add_u32_e32 v2, v1, v2
	v_and_b32_e32 v2, 0xfffffc00, v2
	v_sub_u32_e32 v1, v1, v2
	v_lshrrev_b32_e32 v2, 4, v1
	v_ashrrev_i32_e32 v8, 31, v16
	v_bitop3_b32 v1, v2, v1, 32 bitop3:0x6c
	v_lshrrev_b32_e32 v8, 26, v8
	v_ashrrev_i32_e32 v2, 31, v1
	v_add_u32_e32 v8, v16, v8
	v_lshrrev_b32_e32 v2, 26, v2
	v_ashrrev_i32_e32 v21, 6, v8
	v_add_u32_e32 v2, v1, v2
	v_lshlrev_b32_e32 v8, 3, v21
	v_ashrrev_i32_e32 v20, 6, v2
	v_and_b32_e32 v8, -16, v8
	v_add_u32_e32 v8, v20, v8
	v_and_b32_e32 v9, 3, v20
	s_mov_b32 s100, s27
	v_readlane_b32 s101, v255, 9
	s_cmp_eq_u32 s101, 0
	s_cbranch_scc1 .Lup_u0_std
	s_cmpk_lt_i32 s27, 0x80
	s_cbranch_scc1 .Lup_u0_std
	s_cmp_eq_u32 s101, 1
	s_cbranch_scc0 .Lup_u0_B
	s_or_b32 s100, s27, 8
	s_bitcmp1_b32 s27, 3
	s_cselect_b32 s101, 0, 0x200
	s_add_i32 s100, s100, s101
	s_branch .Lup_u0_std
.Lup_u0_B:
	s_bitcmp1_b32 s27, 3
	s_cselect_b32 s101, 0x480, 0
	s_add_i32 s100, s27, s101
.Lup_u0_std:
	s_ashr_i32 s34, s27, 31
	v_and_or_b32 v9, v8, s0, v9
	s_lshr_b32 s0, s34, 29
	s_add_i32 s0, s100, s0
	s_ashr_i32 s11, s9, 6
	s_ashr_i32 s1, s0, 3
	s_and_b32 s0, s0, -8
	s_ashr_i32 s12, s9, 8
	s_lshl_b32 s10, s11, 10
	s_sub_i32 s0, s100, s0
	s_cmp_lt_i32 s0, 0
	s_movk_i32 s2, 0xb1
	s_cselect_b32 s2, s2, 0xb0
	s_mul_i32 s0, s2, s0
	s_add_i32 s0, s0, s1
	s_mul_hi_i32 s1, s0, 0x2e8ba2e9
	s_lshr_b32 s2, s1, 31
	s_ashr_i32 s1, s1, 5
	s_add_i32 s1, s1, s2
	s_lshl_b32 s2, s1, 3
	s_mulk_i32 s1, 0xb0
	s_sub_i32 s0, s0, s1
	s_bfe_u32 s1, s0, 0x3001c
	s_add_i32 s1, s0, s1
	s_sext_i32_i16 s3, s1
	s_and_b32 s1, s1, 0xfff8
	s_sub_i32 s0, s0, s1
	s_sext_i32_i16 s0, s0
	s_lshr_b32 s8, s3, 3
	s_add_i32 s18, s2, s0
	s_ashr_i32 s19, s18, 31
	s_bfe_i64 s[2:3], s[8:9], 0x100000
	s_lshl_b64 s[0:1], s[18:19], 20
	s_lshl_b64 s[2:3], s[2:3], 20
	s_add_u32 s20, s30, s2
	s_addc_u32 s21, s31, s3
	s_add_i32 s35, s72, 0x10000
	v_lshrrev_b32_e32 v10, 2, v8
	v_lshlrev_b32_e32 v11, 1, v8
	v_and_b32_e32 v2, 0xc0, v2
	s_add_i32 s42, s35, s10
	v_and_b32_e32 v10, 4, v10
	v_and_b32_e32 v11, 24, v11
	v_sub_u32_e32 v1, v1, v2
	s_add_i32 s43, s42, 0x2000
	v_or3_b32 v9, v9, v10, v11
	v_lshlrev_b32_e32 v10, 5, v21
	v_ashrrev_i16_sdwa v1, v228, sext(v1) dst_sel:DWORD dst_unused:UNUSED_PAD src0_sel:DWORD src1_sel:BYTE_0
	s_add_u32 s2, s20, 0x80000
	v_and_b32_e32 v10, 32, v10
	v_bfe_i32 v22, v1, 0, 16
	s_addc_u32 s3, s21, 0
	s_add_i32 s44, s72, 0x14000
	v_add_lshl_u32 v1, v10, v22, 1
	s_add_i32 s45, s44, s10
	v_lshl_add_u32 v2, v9, 12, v1
	s_mov_b32 m0, s42
	s_add_i32 s46, s45, 0x2000
	global_load_lds_dwordx4 v2, s[20:21]
	s_mov_b32 m0, s43
	s_add_u32 s22, s28, s0
	global_load_lds_dwordx4 v172, s[20:21]
	s_mov_b32 m0, s45
	s_addc_u32 s23, s29, s1
	s_add_i32 s47, s72, s10
	global_load_lds_dwordx4 v2, s[2:3]
	s_mov_b32 m0, s46
	s_add_i32 s48, s47, 0x2000
	v_lshl_add_u32 v176, v8, 12, v1
	global_load_lds_dwordx4 v172, s[2:3]
	s_mov_b32 m0, s47
	s_add_u32 s0, s22, 0x80000
	global_load_lds_dwordx4 v176, s[22:23]
	s_mov_b32 m0, s48
	s_addc_u32 s1, s23, 0
	s_add_i32 s49, s47, 0x4000
	global_load_lds_dwordx4 v174, s[22:23]
	s_mov_b32 m0, s49
	s_add_i32 s50, s47, 0x6000
	global_load_lds_dwordx4 v176, s[0:1]
	s_mov_b32 m0, s50
	v_mov_b32_e32 v173, v3
	global_load_lds_dwordx4 v174, s[0:1]
	v_mov_b32_e32 v177, v3
	v_mov_b32_e32 v175, v3
	s_cmp_eq_u32 s12, 1
	v_lshl_add_u64 v[14:15], s[20:21], 0, v[2:3]
	v_lshl_add_u64 v[12:13], s[20:21], 0, v[172:173]
	v_lshl_add_u64 v[8:9], s[22:23], 0, v[176:177]
	s_cselect_b64 s[0:1], -1, 0
	s_cmp_lg_u32 s12, 1
	v_lshl_add_u64 v[10:11], s[22:23], 0, v[174:175]
	s_cbranch_scc1 .LBB0_1914
	s_barrier

.LBB0_1917:
	s_add_i32 s60, s60, 1
	s_mul_i32 s11, s60, s61
	s_mul_hi_u32 s13, s60, s26
	s_add_i32 s13, s13, s11
	s_mul_i32 s11, s60, s26
	s_add_u32 s14, s11, s27
	s_addc_u32 s15, s13, s34
	v_readlane_b32 s100, v255, 9
	s_cmp_eq_u32 s100, 0
	s_cbranch_scc1 .Lup_k_std
	s_cmp_eq_u32 s100, 1
	s_cbranch_scc1 .Lup_k_stop
	s_cmpk_lt_i32 s27, 0x80
	s_cbranch_scc0 .Lup_k_hi
	s_cmp_eq_u32 s60, 5
	s_cbranch_scc1 .Lup_k_stop
	s_branch .Lup_k_std
.Lup_k_hi:
	s_bitcmp1_b32 s27, 3
	s_cbranch_scc0 .Lup_k_std
	s_cmp_eq_u32 s60, 2
	s_cbranch_scc0 .Lup_k_std
	s_add_i32 s14, s27, 0x478
	s_mov_b32 s15, 0
	s_branch .Lup_k_std
.Lup_k_stop:
	s_mov_b32 s14, 0x10000
	s_mov_b32 s15, 0
.Lup_k_std:
	v_mov_b64_e32 v[4:5], 0x580
	v_cmp_lt_i64_e64 s[40:41], s[14:15], v[4:5]
	v_mov_b64_e32 v[4:5], 0x57f
	v_cmp_gt_i64_e32 vcc, s[14:15], v[4:5]
	s_cbranch_vccnz .LBB0_1919
	s_ashr_i32 s10, s14, 31
	s_lshr_b32 s10, s10, 29
	s_add_i32 s10, s14, s10
	s_ashr_i32 s11, s10, 3
	s_and_b32 s10, s10, -8
	s_sub_i32 s10, s14, s10
	s_cmp_lt_i32 s10, 0
	s_movk_i32 s12, 0xb1
	s_cselect_b32 s12, s12, 0xb0
	s_mul_i32 s10, s12, s10
	s_add_i32 s10, s10, s11
	s_mul_hi_i32 s11, s10, 0x2e8ba2e9
	s_lshr_b32 s12, s11, 31
	s_ashr_i32 s11, s11, 5
	s_add_i32 s11, s11, s12
	s_lshl_b32 s12, s11, 3
	s_sub_i32 s13, 64, s12
	s_min_i32 s13, s13, 8
	s_abs_i32 s14, s13
	v_cvt_f32_u32_e32 v4, s14
	s_sub_i32 s16, 0, s14
	s_mulk_i32 s11, 0xb0
	s_sub_i32 s11, s10, s11
	v_rcp_iflag_f32_e32 v4, v4
	s_abs_i32 s10, s11
	s_xor_b32 s15, s11, s13
	s_ashr_i32 s15, s15, 31
	v_mul_f32_e32 v4, 0x4f7ffffe, v4
	v_cvt_u32_f32_e32 v4, v4
	s_nop 0
	v_readfirstlane_b32 s17, v4
	s_mul_i32 s16, s16, s17
	s_mul_hi_u32 s16, s17, s16
	s_add_i32 s17, s17, s16
	s_mul_hi_u32 s16, s10, s17
	s_mul_i32 s17, s16, s14
	s_sub_i32 s10, s10, s17
	s_add_i32 s24, s16, 1
	s_sub_i32 s17, s10, s14
	s_cmp_ge_u32 s10, s14
	s_cselect_b32 s16, s24, s16
	s_cselect_b32 s10, s17, s10
	s_add_i32 s17, s16, 1
	s_cmp_ge_u32 s10, s14
	s_cselect_b32 s10, s17, s16
	s_xor_b32 s10, s10, s15
	s_sub_i32 s10, s10, s15
	s_mul_i32 s13, s10, s13
	s_sub_i32 s11, s11, s13
	s_add_i32 s12, s11, s12

.LBB0_1927:
	v_readlane_b32 s100, v255, 9
	s_cmp_lg_u32 s100, 1
	s_cbranch_scc1 .Lup_notA
	s_mov_b32 s100, 2
	v_writelane_b32 v255, s100, 9
	s_branch .LBB0_1854
.Lup_notA:
	s_mov_b32 s100, 0
	v_writelane_b32 v255, s100, 9
	v_readlane_b32 s0, v253, 26
	s_add_i32 s16, s0, 12
	s_cmp_ge_i32 s16, s91
	s_cbranch_scc1 .LBB0_1981
	s_waitcnt vmcnt(0)
	s_waitcnt vmcnt(0) lgkmcnt(0)
	s_barrier
	s_mov_b64 s[0:1], exec
	v_readlane_b32 s2, v252, 3
	v_readlane_b32 s3, v252, 4
	s_and_b64 s[2:3], s[0:1], s[2:3]
	s_mov_b64 exec, s[2:3]
	s_cbranch_execz .LBB0_1980
	v_readlane_b32 s2, v253, 15
	s_waitcnt vmcnt(0) expcnt(0) lgkmcnt(0)
	s_nop 0
	v_mov_b32_e32 v1, s2
	ds_read_b32 v4, v1
	v_readlane_b32 s2, v253, 16
	s_waitcnt lgkmcnt(0)
	v_cmp_ne_u32_e32 vcc, 0, v4
	v_mov_b32_e32 v1, s2
	ds_read_b32 v2, v1
	s_cbranch_vccnz .LBB0_1944
	v_readlane_b32 s4, v252, 1
	v_readlane_b32 s5, v252, 2
	s_load_dwordx2 s[2:3], s[4:5], 0x4
	v_readlane_b32 s4, v252, 0
	s_mov_b32 s9, 1
	s_waitcnt lgkmcnt(0)
	s_mul_i32 s8, s2, s4
	s_mul_i32 s8, s8, s3
	s_branch .LBB0_1932
